# gate|up -> down expert GEMMs: grid barrier replaced by per-slot-tile completion counters (write-through act stores, one polling wave), down units re-dealt so blocks with a third gate|up unit take fewe
# speedup vs baseline: 1.0633x; 1.0340x over previous
.LBB0_1002:
	s_add_i32 s2, s20, s22
	s_add_i32 s23, s2, 4
	s_and_b32 s23, s23, 31
	s_lshl_b32 s36, s23, 17
	v_add_u32_e32 v105, v166, v161
	s_nop 0
	s_nop 1
	v_lshl_add_u64 v[136:137], v[110:111], 0, s[36:37]
	v_add_co_u32_e32 v140, vcc, 0x1000, v136
	s_nop 1
	v_addc_co_u32_e32 v141, vcc, 0, v137, vcc
	global_load_dwordx4 v[128:131], v[136:137], off
	global_load_dwordx4 v[132:135], v[136:137], off offset:2048
	global_load_dwordx4 v[136:139], v[140:141], off
	global_load_dwordx4 v[140:143], v[140:141], off offset:2048
	ds_read_b128 v[146:149], v105
	ds_read_b128 v[150:153], v105 offset:2048
	ds_read_b128 v[154:157], v105 offset:8192
	ds_read_b128 v[170:173], v105 offset:10240
	v_add_u32_e32 v105, v167, v161
	ds_read_b128 v[174:177], v105
	ds_read_b128 v[178:181], v105 offset:2048
	s_setprio 1
	s_waitcnt lgkmcnt(1)
	v_mfma_f32_16x16x32_bf16 v[76:79], v[146:149], v[174:177], v[76:79]
	v_mfma_f32_16x16x32_bf16 v[68:71], v[150:153], v[174:177], v[68:71]
	v_mfma_f32_16x16x32_bf16 v[72:75], v[154:157], v[174:177], v[72:75]
	v_mfma_f32_16x16x32_bf16 v[64:67], v[170:173], v[174:177], v[64:67]
	s_setprio 0
	ds_read_b128 v[174:177], v105 offset:4096
	s_setprio 1
	s_waitcnt lgkmcnt(1)
	v_mfma_f32_16x16x32_bf16 v[56:59], v[146:149], v[178:181], v[56:59]
	v_mfma_f32_16x16x32_bf16 v[48:51], v[150:153], v[178:181], v[48:51]
	v_mfma_f32_16x16x32_bf16 v[60:63], v[154:157], v[178:181], v[60:63]
	v_mfma_f32_16x16x32_bf16 v[52:55], v[170:173], v[178:181], v[52:55]
	s_setprio 0
	ds_read_b128 v[178:181], v105 offset:6144
	s_setprio 1
	s_waitcnt lgkmcnt(1)
	v_mfma_f32_16x16x32_bf16 v[40:43], v[146:149], v[174:177], v[40:43]
	v_mfma_f32_16x16x32_bf16 v[32:35], v[150:153], v[174:177], v[32:35]
	v_mfma_f32_16x16x32_bf16 v[44:47], v[154:157], v[174:177], v[44:47]
	v_mfma_f32_16x16x32_bf16 v[36:39], v[170:173], v[174:177], v[36:39]
	s_setprio 0
	ds_read_b128 v[174:177], v105 offset:8192
	s_setprio 1
	s_waitcnt lgkmcnt(1)
	v_mfma_f32_16x16x32_bf16 v[24:27], v[146:149], v[178:181], v[24:27]
	v_mfma_f32_16x16x32_bf16 v[16:19], v[150:153], v[178:181], v[16:19]
	v_mfma_f32_16x16x32_bf16 v[28:31], v[154:157], v[178:181], v[28:31]
	v_mfma_f32_16x16x32_bf16 v[20:23], v[170:173], v[178:181], v[20:23]
	s_setprio 0
	s_setprio 1
	s_waitcnt lgkmcnt(0)
	v_mfma_f32_16x16x32_bf16 v[8:11], v[146:149], v[174:177], v[8:11]
	v_mfma_f32_16x16x32_bf16 v[0:3], v[150:153], v[174:177], v[0:3]
	v_mfma_f32_16x16x32_bf16 v[12:15], v[154:157], v[174:177], v[12:15]
	v_mfma_f32_16x16x32_bf16 v[4:7], v[170:173], v[174:177], v[4:7]
	s_setprio 0
	v_add_u32_e32 v107, v166, v160
	ds_read_b128 v[146:149], v107
	ds_read_b128 v[150:153], v107 offset:2048
	ds_read_b128 v[154:157], v107 offset:8192
	ds_read_b128 v[170:173], v107 offset:10240
	v_add_u32_e32 v107, v167, v160
	ds_read_b128 v[174:177], v107
	ds_read_b128 v[178:181], v107 offset:2048
	s_setprio 1
	s_waitcnt lgkmcnt(1)
	v_mfma_f32_16x16x32_bf16 v[76:79], v[146:149], v[174:177], v[76:79]
	v_mfma_f32_16x16x32_bf16 v[68:71], v[150:153], v[174:177], v[68:71]
	v_mfma_f32_16x16x32_bf16 v[72:75], v[154:157], v[174:177], v[72:75]
	v_mfma_f32_16x16x32_bf16 v[64:67], v[170:173], v[174:177], v[64:67]
	s_setprio 0
	ds_read_b128 v[174:177], v107 offset:4096
	s_setprio 1
	s_waitcnt lgkmcnt(1)
	v_mfma_f32_16x16x32_bf16 v[56:59], v[146:149], v[178:181], v[56:59]
	v_mfma_f32_16x16x32_bf16 v[48:51], v[150:153], v[178:181], v[48:51]
	v_mfma_f32_16x16x32_bf16 v[60:63], v[154:157], v[178:181], v[60:63]
	v_mfma_f32_16x16x32_bf16 v[52:55], v[170:173], v[178:181], v[52:55]
	s_setprio 0
	ds_read_b128 v[178:181], v107 offset:6144
	s_setprio 1
	s_waitcnt lgkmcnt(1)
	v_mfma_f32_16x16x32_bf16 v[40:43], v[146:149], v[174:177], v[40:43]
	v_mfma_f32_16x16x32_bf16 v[32:35], v[150:153], v[174:177], v[32:35]
	v_mfma_f32_16x16x32_bf16 v[44:47], v[154:157], v[174:177], v[44:47]
	v_mfma_f32_16x16x32_bf16 v[36:39], v[170:173], v[174:177], v[36:39]
	s_setprio 0
	ds_read_b128 v[174:177], v107 offset:8192
	s_setprio 1
	s_waitcnt lgkmcnt(1)
	v_mfma_f32_16x16x32_bf16 v[24:27], v[146:149], v[178:181], v[24:27]
	v_mfma_f32_16x16x32_bf16 v[16:19], v[150:153], v[178:181], v[16:19]
	v_mfma_f32_16x16x32_bf16 v[28:31], v[154:157], v[178:181], v[28:31]
	v_mfma_f32_16x16x32_bf16 v[20:23], v[170:173], v[178:181], v[20:23]
	s_setprio 0
	s_setprio 1
	s_waitcnt lgkmcnt(0)
	v_mfma_f32_16x16x32_bf16 v[8:11], v[146:149], v[174:177], v[8:11]
	v_mfma_f32_16x16x32_bf16 v[0:3], v[150:153], v[174:177], v[0:3]
	v_mfma_f32_16x16x32_bf16 v[12:15], v[154:157], v[174:177], v[12:15]
	v_mfma_f32_16x16x32_bf16 v[4:7], v[170:173], v[174:177], v[4:7]
	s_setprio 0
	s_waitcnt vmcnt(8)
	ds_write_b128 v165, v[80:83] offset:40960
	s_waitcnt vmcnt(7)
	ds_write_b128 v165, v[84:87] offset:49152
	s_waitcnt vmcnt(6)
	ds_write_b128 v165, v[88:91] offset:57344
	s_waitcnt vmcnt(5)
	ds_write_b128 v168, v[92:95] offset:24576
	s_waitcnt vmcnt(4)
	ds_write_b128 v168, v[96:99] offset:32768
	v_permlane32_swap_b32_e32 v112, v114
	v_permlane32_swap_b32_e32 v113, v115
	v_permlane32_swap_b32_e32 v116, v118
	v_permlane32_swap_b32_e32 v117, v119
	v_permlane32_swap_b32_e32 v120, v122
	v_permlane32_swap_b32_e32 v121, v123
	v_permlane32_swap_b32_e32 v124, v126
	v_permlane32_swap_b32_e32 v125, v127
	v_cvt_pk_bf16_f32 v80, v112, v116
	v_cvt_pk_bf16_f32 v81, v120, v124
	v_cvt_pk_bf16_f32 v82, v114, v118
	v_cvt_pk_bf16_f32 v83, v122, v126
	v_cvt_pk_bf16_f32 v84, v113, v117
	v_cvt_pk_bf16_f32 v85, v121, v125
	v_cvt_pk_bf16_f32 v86, v115, v119
	v_cvt_pk_bf16_f32 v87, v123, v127
	v_add_u32_e32 v88, s18, v164
	s_lshl_b32 s36, s23, 7
	v_add_u32_e32 v89, s18, v163
	ds_write_b128 v88, v[80:83]
	ds_write_b128 v89, v[84:87]
	v_lshl_add_u64 v[80:81], v[108:109], 0, s[36:37]
	v_add_co_u32_e32 v84, vcc, s53, v80
	s_add_i32 s2, s2, 5
	s_nop 0
	v_addc_co_u32_e32 v85, vcc, 0, v81, vcc
	v_add_co_u32_e32 v88, vcc, s82, v80
	s_and_b32 s2, s2, 31
	s_nop 0
	v_addc_co_u32_e32 v89, vcc, 0, v81, vcc
	v_add_co_u32_e32 v92, vcc, s47, v80
	s_lshl_b32 s36, s2, 17
	s_nop 0
	v_addc_co_u32_e32 v93, vcc, 0, v81, vcc
	v_add_co_u32_e32 v96, vcc, s49, v80
	s_nop 0
	v_addc_co_u32_e32 v97, vcc, 0, v81, vcc
	global_load_dwordx4 v[80:83], v[80:81], off
	s_nop 0
	global_load_dwordx4 v[84:87], v[84:85], off
	s_nop 0
	global_load_dwordx4 v[88:91], v[88:89], off
	s_nop 0
	global_load_dwordx4 v[92:95], v[92:93], off
	s_nop 0
	global_load_dwordx4 v[96:99], v[96:97], off
	v_lshl_add_u64 v[120:121], v[110:111], 0, s[36:37]
	v_add_co_u32_e32 v124, vcc, 0x1000, v120
	s_nop 1
	v_addc_co_u32_e32 v125, vcc, 0, v121, vcc
	s_waitcnt lgkmcnt(0)
	s_nop 0
	s_barrier
	global_load_dwordx4 v[112:115], v[120:121], off
	global_load_dwordx4 v[116:119], v[120:121], off offset:2048
	global_load_dwordx4 v[120:123], v[124:125], off
	global_load_dwordx4 v[124:127], v[124:125], off offset:2048
	v_add_u32_e32 v144, v169, v161
	ds_read_b128 v[146:149], v144
	ds_read_b128 v[150:153], v144 offset:2048
	ds_read_b128 v[154:157], v144 offset:8192
	ds_read_b128 v[170:173], v144 offset:10240
	ds_read_b128 v[174:177], v105 offset:40960
	ds_read_b128 v[178:181], v105 offset:43008
	s_setprio 1
	s_waitcnt lgkmcnt(1)
	v_mfma_f32_16x16x32_bf16 v[76:79], v[146:149], v[174:177], v[76:79]
	v_mfma_f32_16x16x32_bf16 v[68:71], v[150:153], v[174:177], v[68:71]
	v_mfma_f32_16x16x32_bf16 v[72:75], v[154:157], v[174:177], v[72:75]
	v_mfma_f32_16x16x32_bf16 v[64:67], v[170:173], v[174:177], v[64:67]
	s_setprio 0
	ds_read_b128 v[174:177], v105 offset:45056
	s_setprio 1
	s_waitcnt lgkmcnt(1)
	v_mfma_f32_16x16x32_bf16 v[56:59], v[146:149], v[178:181], v[56:59]
	v_mfma_f32_16x16x32_bf16 v[48:51], v[150:153], v[178:181], v[48:51]
	v_mfma_f32_16x16x32_bf16 v[60:63], v[154:157], v[178:181], v[60:63]
	v_mfma_f32_16x16x32_bf16 v[52:55], v[170:173], v[178:181], v[52:55]
	s_setprio 0
	ds_read_b128 v[178:181], v105 offset:47104
	s_setprio 1
	s_waitcnt lgkmcnt(1)
	v_mfma_f32_16x16x32_bf16 v[40:43], v[146:149], v[174:177], v[40:43]
	v_mfma_f32_16x16x32_bf16 v[32:35], v[150:153], v[174:177], v[32:35]
	v_mfma_f32_16x16x32_bf16 v[44:47], v[154:157], v[174:177], v[44:47]
	v_mfma_f32_16x16x32_bf16 v[36:39], v[170:173], v[174:177], v[36:39]
	s_setprio 0
	ds_read_b128 v[174:177], v105 offset:49152
	s_setprio 1
	s_waitcnt lgkmcnt(1)
	v_mfma_f32_16x16x32_bf16 v[24:27], v[146:149], v[178:181], v[24:27]
	v_mfma_f32_16x16x32_bf16 v[16:19], v[150:153], v[178:181], v[16:19]
	v_mfma_f32_16x16x32_bf16 v[28:31], v[154:157], v[178:181], v[28:31]
	v_mfma_f32_16x16x32_bf16 v[20:23], v[170:173], v[178:181], v[20:23]
	s_setprio 0
	s_setprio 1
	s_waitcnt lgkmcnt(0)
	v_mfma_f32_16x16x32_bf16 v[8:11], v[146:149], v[174:177], v[8:11]
	v_mfma_f32_16x16x32_bf16 v[0:3], v[150:153], v[174:177], v[0:3]
	v_mfma_f32_16x16x32_bf16 v[12:15], v[154:157], v[174:177], v[12:15]
	v_mfma_f32_16x16x32_bf16 v[4:7], v[170:173], v[174:177], v[4:7]
	s_setprio 0
	v_add_u32_e32 v105, v169, v160
	ds_read_b128 v[146:149], v105
	ds_read_b128 v[150:153], v105 offset:2048
	ds_read_b128 v[154:157], v105 offset:8192
	ds_read_b128 v[170:173], v105 offset:10240
	ds_read_b128 v[174:177], v107 offset:40960
	ds_read_b128 v[178:181], v107 offset:43008
	s_setprio 1
	s_waitcnt lgkmcnt(1)
	v_mfma_f32_16x16x32_bf16 v[76:79], v[146:149], v[174:177], v[76:79]
	v_mfma_f32_16x16x32_bf16 v[68:71], v[150:153], v[174:177], v[68:71]
	v_mfma_f32_16x16x32_bf16 v[72:75], v[154:157], v[174:177], v[72:75]
	v_mfma_f32_16x16x32_bf16 v[64:67], v[170:173], v[174:177], v[64:67]
	s_setprio 0
	ds_read_b128 v[174:177], v107 offset:45056
	s_setprio 1
	s_waitcnt lgkmcnt(1)
	v_mfma_f32_16x16x32_bf16 v[56:59], v[146:149], v[178:181], v[56:59]
	v_mfma_f32_16x16x32_bf16 v[48:51], v[150:153], v[178:181], v[48:51]
	v_mfma_f32_16x16x32_bf16 v[60:63], v[154:157], v[178:181], v[60:63]
	v_mfma_f32_16x16x32_bf16 v[52:55], v[170:173], v[178:181], v[52:55]
	s_setprio 0
	ds_read_b128 v[178:181], v107 offset:47104
	s_setprio 1
	s_waitcnt lgkmcnt(1)
	v_mfma_f32_16x16x32_bf16 v[40:43], v[146:149], v[174:177], v[40:43]
	v_mfma_f32_16x16x32_bf16 v[32:35], v[150:153], v[174:177], v[32:35]
	v_mfma_f32_16x16x32_bf16 v[44:47], v[154:157], v[174:177], v[44:47]
	v_mfma_f32_16x16x32_bf16 v[36:39], v[170:173], v[174:177], v[36:39]
	s_setprio 0
	ds_read_b128 v[174:177], v107 offset:49152
	s_setprio 1
	s_waitcnt lgkmcnt(1)
	v_mfma_f32_16x16x32_bf16 v[24:27], v[146:149], v[178:181], v[24:27]
	v_mfma_f32_16x16x32_bf16 v[16:19], v[150:153], v[178:181], v[16:19]
	v_mfma_f32_16x16x32_bf16 v[28:31], v[154:157], v[178:181], v[28:31]
	v_mfma_f32_16x16x32_bf16 v[20:23], v[170:173], v[178:181], v[20:23]
	s_setprio 0
	s_setprio 1
	s_waitcnt lgkmcnt(0)
	v_mfma_f32_16x16x32_bf16 v[8:11], v[146:149], v[174:177], v[8:11]
	v_mfma_f32_16x16x32_bf16 v[0:3], v[150:153], v[174:177], v[0:3]
	v_mfma_f32_16x16x32_bf16 v[12:15], v[154:157], v[174:177], v[12:15]
	v_mfma_f32_16x16x32_bf16 v[4:7], v[170:173], v[174:177], v[4:7]
	s_setprio 0
	s_lshl_b32 s36, s2, 7
	s_waitcnt vmcnt(8)
	ds_write_b128 v165, v[80:83]
	s_waitcnt vmcnt(7)
	ds_write_b128 v165, v[84:87] offset:8192
	s_waitcnt vmcnt(6)
	ds_write_b128 v165, v[88:91] offset:16384
	s_waitcnt vmcnt(5)
	ds_write_b128 v165, v[92:95] offset:24576
	s_waitcnt vmcnt(4)
	ds_write_b128 v165, v[96:99] offset:32768
	v_permlane32_swap_b32_e32 v128, v130
	v_permlane32_swap_b32_e32 v129, v131
	v_permlane32_swap_b32_e32 v132, v134
	v_permlane32_swap_b32_e32 v133, v135
	v_permlane32_swap_b32_e32 v136, v138
	v_permlane32_swap_b32_e32 v137, v139
	v_permlane32_swap_b32_e32 v140, v142
	v_permlane32_swap_b32_e32 v141, v143
	v_cvt_pk_bf16_f32 v80, v128, v132
	v_cvt_pk_bf16_f32 v81, v136, v140
	v_cvt_pk_bf16_f32 v82, v130, v134
	v_cvt_pk_bf16_f32 v83, v138, v142
	v_cvt_pk_bf16_f32 v84, v129, v133
	v_cvt_pk_bf16_f32 v85, v137, v141
	v_cvt_pk_bf16_f32 v86, v131, v135
	v_cvt_pk_bf16_f32 v87, v139, v143
	v_lshl_add_u64 v[96:97], v[108:109], 0, s[36:37]
	ds_write_b128 v101, v[80:83]
	ds_write_b128 v103, v[84:87]
	v_add_co_u32_e32 v84, vcc, s53, v96
	global_load_dwordx4 v[80:83], v[96:97], off
	s_nop 0
	v_addc_co_u32_e32 v85, vcc, 0, v97, vcc
	v_add_co_u32_e32 v88, vcc, s82, v96
	global_load_dwordx4 v[84:87], v[84:85], off
	s_nop 0
	v_addc_co_u32_e32 v89, vcc, 0, v97, vcc
	v_add_co_u32_e32 v92, vcc, s47, v96
	global_load_dwordx4 v[88:91], v[88:89], off
	s_nop 0
	v_addc_co_u32_e32 v93, vcc, 0, v97, vcc
	global_load_dwordx4 v[92:95], v[92:93], off
	v_add_co_u32_e32 v96, vcc, s49, v96
	s_add_i32 s22, s22, 2
	s_nop 0
	v_addc_co_u32_e32 v97, vcc, 0, v97, vcc
	global_load_dwordx4 v[96:99], v[96:97], off
	s_cmp_gt_u32 s22, 29
	s_waitcnt lgkmcnt(0)
	s_barrier
	s_cbranch_scc0 .LBB0_1002
	s_waitcnt vmcnt(4)
	v_mul_f32_e32 v82, 0xbfb8aa3b, v76
	v_mul_f32_e32 v83, 0xbfb8aa3b, v77
	v_exp_f32_e32 v82, v82
	v_exp_f32_e32 v83, v83
	v_mov_b32_e32 v80, v145
	s_mov_b64 s[22:23], s[10:11]
	v_add_f32_e32 v82, 1.0, v82
	v_add_f32_e32 v83, 1.0, v83
	v_rcp_f32_e32 v82, v82
	v_rcp_f32_e32 v83, v83
	s_mov_b64 s[24:25], 0
	s_lshl_b64 s[14:15], s[14:15], 1
	v_pk_mul_f32 v[76:77], v[76:77], v[82:83]
	s_add_u32 s2, s22, s14
	v_pk_mul_f32 v[72:73], v[72:73], v[76:77]
	v_mul_f32_e32 v76, 0xbfb8aa3b, v78
	v_mul_f32_e32 v77, 0xbfb8aa3b, v79
	v_exp_f32_e32 v76, v76
	v_exp_f32_e32 v77, v77
	v_cvt_pk_bf16_f32 v72, v72, v73
	s_addc_u32 s15, s23, s15
	v_add_f32_e32 v76, 1.0, v76
	v_add_f32_e32 v77, 1.0, v77
	v_rcp_f32_e32 v76, v76
	v_rcp_f32_e32 v77, v77
	s_add_u32 s14, s2, s19
	s_addc_u32 s15, s15, 0
	v_mov_b32_e32 v105, v145
	v_pk_mul_f32 v[76:77], v[78:79], v[76:77]
	v_add3_u32 v144, s21, v162, v80
	v_pk_mul_f32 v[74:75], v[74:75], v[76:77]
	v_lshl_add_u64 v[80:81], s[14:15], 0, v[104:105]
	v_cvt_pk_bf16_f32 v73, v74, v75
	v_mul_f32_e32 v74, 0xbfb8aa3b, v68
	v_mul_f32_e32 v75, 0xbfb8aa3b, v69
	v_exp_f32_e32 v74, v74
	v_exp_f32_e32 v75, v75
	v_mov_b32_e32 v107, v145
	v_lshl_add_u64 v[80:81], v[80:81], 0, v[106:107]
	v_add_f32_e32 v74, 1.0, v74
	v_add_f32_e32 v75, 1.0, v75
	v_rcp_f32_e32 v74, v74
	v_rcp_f32_e32 v75, v75
	s_nop 0
	v_pk_mul_f32 v[68:69], v[68:69], v[74:75]
	s_nop 0
	v_pk_mul_f32 v[64:65], v[64:65], v[68:69]
	v_mul_f32_e32 v68, 0xbfb8aa3b, v70
	v_mul_f32_e32 v69, 0xbfb8aa3b, v71
	v_exp_f32_e32 v68, v68
	v_exp_f32_e32 v69, v69
	v_cvt_pk_bf16_f32 v74, v64, v65
	v_lshlrev_b64 v[64:65], 10, v[144:145]
	v_add_f32_e32 v68, 1.0, v68
	v_add_f32_e32 v69, 1.0, v69
	v_rcp_f32_e32 v68, v68
	v_rcp_f32_e32 v69, v69
	v_permlane16_swap_b32_e32 v72, v74
	v_lshl_add_u64 v[64:65], v[80:81], 0, v[64:65]
	v_pk_mul_f32 v[68:69], v[70:71], v[68:69]
	s_nop 0
	v_pk_mul_f32 v[66:67], v[66:67], v[68:69]
	s_nop 0
	v_cvt_pk_bf16_f32 v75, v66, v67
	s_nop 1
	v_permlane16_swap_b32_e32 v73, v75
	global_store_dwordx4 v[64:65], v[72:75], off sc0 sc1
	v_mul_f32_e32 v65, 0xbfb8aa3b, v56
	v_exp_f32_e32 v65, v65
	v_add_u32_e32 v64, 16, v144
	v_add_f32_e32 v65, 1.0, v65
	v_rcp_f32_e32 v66, v65
	v_mul_f32_e32 v65, 0xbfb8aa3b, v57
	v_exp_f32_e32 v65, v65
	s_nop 0
	v_add_f32_e32 v65, 1.0, v65
	v_rcp_f32_e32 v67, v65
	v_mov_b32_e32 v65, v145
	v_pk_mul_f32 v[56:57], v[56:57], v[66:67]
	s_nop 0
	v_pk_mul_f32 v[56:57], v[60:61], v[56:57]
	v_mul_f32_e32 v60, 0xbfb8aa3b, v58
	v_mul_f32_e32 v61, 0xbfb8aa3b, v59
	v_exp_f32_e32 v60, v60
	v_exp_f32_e32 v61, v61
	v_cvt_pk_bf16_f32 v56, v56, v57
	v_add_f32_e32 v60, 1.0, v60
	v_add_f32_e32 v61, 1.0, v61
	v_rcp_f32_e32 v60, v60
	v_rcp_f32_e32 v61, v61
	s_nop 0
	v_pk_mul_f32 v[58:59], v[58:59], v[60:61]
	s_nop 0
	v_pk_mul_f32 v[58:59], v[62:63], v[58:59]
	s_nop 0
	v_cvt_pk_bf16_f32 v57, v58, v59
	v_mul_f32_e32 v58, 0xbfb8aa3b, v48
	v_mul_f32_e32 v59, 0xbfb8aa3b, v49
	v_exp_f32_e32 v58, v58
	v_exp_f32_e32 v59, v59
	v_add_f32_e32 v58, 1.0, v58
	v_add_f32_e32 v59, 1.0, v59
	v_rcp_f32_e32 v58, v58
	v_rcp_f32_e32 v59, v59
	s_nop 0
	v_pk_mul_f32 v[48:49], v[48:49], v[58:59]
	s_nop 0
	v_pk_mul_f32 v[48:49], v[52:53], v[48:49]
	v_mul_f32_e32 v52, 0xbfb8aa3b, v50
	v_mul_f32_e32 v53, 0xbfb8aa3b, v51
	v_exp_f32_e32 v52, v52
	v_exp_f32_e32 v53, v53
	v_cvt_pk_bf16_f32 v58, v48, v49
	v_lshlrev_b64 v[48:49], 10, v[64:65]
	v_add_f32_e32 v52, 1.0, v52
	v_add_f32_e32 v53, 1.0, v53
	v_rcp_f32_e32 v52, v52
	v_rcp_f32_e32 v53, v53
	v_permlane16_swap_b32_e32 v56, v58
	v_lshl_add_u64 v[48:49], v[80:81], 0, v[48:49]
	v_pk_mul_f32 v[50:51], v[50:51], v[52:53]
	s_nop 0
	v_pk_mul_f32 v[50:51], v[54:55], v[50:51]
	s_nop 0
	v_cvt_pk_bf16_f32 v59, v50, v51
	s_nop 1
	v_permlane16_swap_b32_e32 v57, v59
	global_store_dwordx4 v[48:49], v[56:59], off sc0 sc1
	v_mul_f32_e32 v49, 0xbfb8aa3b, v40
	v_exp_f32_e32 v49, v49
	v_add_u32_e32 v48, 32, v144
	v_add_f32_e32 v49, 1.0, v49
	v_rcp_f32_e32 v50, v49
	v_mul_f32_e32 v49, 0xbfb8aa3b, v41
	v_exp_f32_e32 v49, v49
	s_nop 0
	v_add_f32_e32 v49, 1.0, v49
	v_rcp_f32_e32 v51, v49
	v_mov_b32_e32 v49, v145
	v_pk_mul_f32 v[40:41], v[40:41], v[50:51]
	s_nop 0
	v_pk_mul_f32 v[40:41], v[44:45], v[40:41]
	v_mul_f32_e32 v44, 0xbfb8aa3b, v42
	v_mul_f32_e32 v45, 0xbfb8aa3b, v43
	v_exp_f32_e32 v44, v44
	v_exp_f32_e32 v45, v45
	v_cvt_pk_bf16_f32 v40, v40, v41
	v_add_f32_e32 v44, 1.0, v44
	v_add_f32_e32 v45, 1.0, v45
	v_rcp_f32_e32 v44, v44
	v_rcp_f32_e32 v45, v45
	s_nop 0
	v_pk_mul_f32 v[42:43], v[42:43], v[44:45]
	s_nop 0
	v_pk_mul_f32 v[42:43], v[46:47], v[42:43]
	s_nop 0
	v_cvt_pk_bf16_f32 v41, v42, v43
	v_mul_f32_e32 v42, 0xbfb8aa3b, v32
	v_mul_f32_e32 v43, 0xbfb8aa3b, v33
	v_exp_f32_e32 v42, v42
	v_exp_f32_e32 v43, v43
	v_add_f32_e32 v42, 1.0, v42
	v_add_f32_e32 v43, 1.0, v43
	v_rcp_f32_e32 v42, v42
	v_rcp_f32_e32 v43, v43
	s_nop 0
	v_pk_mul_f32 v[32:33], v[32:33], v[42:43]
	s_nop 0
	v_pk_mul_f32 v[32:33], v[36:37], v[32:33]
	v_mul_f32_e32 v36, 0xbfb8aa3b, v34
	v_mul_f32_e32 v37, 0xbfb8aa3b, v35
	v_exp_f32_e32 v36, v36
	v_exp_f32_e32 v37, v37
	v_cvt_pk_bf16_f32 v42, v32, v33
	v_lshlrev_b64 v[32:33], 10, v[48:49]
	v_add_f32_e32 v36, 1.0, v36
	v_add_f32_e32 v37, 1.0, v37
	v_rcp_f32_e32 v36, v36
	v_rcp_f32_e32 v37, v37
	v_permlane16_swap_b32_e32 v40, v42
	v_lshl_add_u64 v[32:33], v[80:81], 0, v[32:33]
	v_pk_mul_f32 v[34:35], v[34:35], v[36:37]
	s_nop 0
	v_pk_mul_f32 v[34:35], v[38:39], v[34:35]
	s_nop 0
	v_cvt_pk_bf16_f32 v43, v34, v35
	s_nop 1
	v_permlane16_swap_b32_e32 v41, v43
	global_store_dwordx4 v[32:33], v[40:43], off sc0 sc1
	v_mul_f32_e32 v33, 0xbfb8aa3b, v24
	v_exp_f32_e32 v33, v33
	v_add_u32_e32 v32, 48, v144
	v_add_u32_e32 v144, 64, v144
	v_add_f32_e32 v33, 1.0, v33
	v_rcp_f32_e32 v34, v33
	v_mul_f32_e32 v33, 0xbfb8aa3b, v25
	v_exp_f32_e32 v33, v33
	s_nop 0
	v_add_f32_e32 v33, 1.0, v33
	v_rcp_f32_e32 v35, v33
	v_mov_b32_e32 v33, v145
	v_pk_mul_f32 v[24:25], v[24:25], v[34:35]
	s_nop 0
	v_pk_mul_f32 v[24:25], v[28:29], v[24:25]
	v_mul_f32_e32 v28, 0xbfb8aa3b, v26
	v_mul_f32_e32 v29, 0xbfb8aa3b, v27
	v_exp_f32_e32 v28, v28
	v_exp_f32_e32 v29, v29
	v_cvt_pk_bf16_f32 v24, v24, v25
	v_add_f32_e32 v28, 1.0, v28
	v_add_f32_e32 v29, 1.0, v29
	v_rcp_f32_e32 v28, v28
	v_rcp_f32_e32 v29, v29
	s_nop 0
	v_pk_mul_f32 v[26:27], v[26:27], v[28:29]
	s_nop 0
	v_pk_mul_f32 v[26:27], v[30:31], v[26:27]
	s_nop 0
	v_cvt_pk_bf16_f32 v25, v26, v27
	v_mul_f32_e32 v26, 0xbfb8aa3b, v16
	v_mul_f32_e32 v27, 0xbfb8aa3b, v17
	v_exp_f32_e32 v26, v26
	v_exp_f32_e32 v27, v27
	v_add_f32_e32 v26, 1.0, v26
	v_add_f32_e32 v27, 1.0, v27
	v_rcp_f32_e32 v26, v26
	v_rcp_f32_e32 v27, v27
	s_nop 0
	v_pk_mul_f32 v[16:17], v[16:17], v[26:27]
	s_nop 0
	v_pk_mul_f32 v[16:17], v[20:21], v[16:17]
	v_mul_f32_e32 v20, 0xbfb8aa3b, v18
	v_mul_f32_e32 v21, 0xbfb8aa3b, v19
	v_exp_f32_e32 v20, v20
	v_exp_f32_e32 v21, v21
	v_cvt_pk_bf16_f32 v26, v16, v17
	v_lshlrev_b64 v[16:17], 10, v[32:33]
	v_add_f32_e32 v20, 1.0, v20
	v_add_f32_e32 v21, 1.0, v21
	v_rcp_f32_e32 v20, v20
	v_rcp_f32_e32 v21, v21
	v_permlane16_swap_b32_e32 v24, v26
	v_lshl_add_u64 v[16:17], v[80:81], 0, v[16:17]
	v_pk_mul_f32 v[18:19], v[18:19], v[20:21]
	s_nop 0
	v_pk_mul_f32 v[18:19], v[22:23], v[18:19]
	s_nop 0
	v_cvt_pk_bf16_f32 v27, v18, v19
	s_nop 1
	v_permlane16_swap_b32_e32 v25, v27
	global_store_dwordx4 v[16:17], v[24:27], off sc0 sc1
	v_mul_f32_e32 v16, 0xbfb8aa3b, v8
	v_mul_f32_e32 v17, 0xbfb8aa3b, v9
	v_exp_f32_e32 v16, v16
	v_exp_f32_e32 v17, v17
	v_add_f32_e32 v16, 1.0, v16
	v_add_f32_e32 v17, 1.0, v17
	v_rcp_f32_e32 v16, v16
	v_rcp_f32_e32 v17, v17
	s_nop 0
	v_pk_mul_f32 v[8:9], v[8:9], v[16:17]
	s_nop 0
	v_pk_mul_f32 v[8:9], v[12:13], v[8:9]
	v_mul_f32_e32 v12, 0xbfb8aa3b, v10
	v_mul_f32_e32 v13, 0xbfb8aa3b, v11
	v_exp_f32_e32 v12, v12
	v_exp_f32_e32 v13, v13
	v_cvt_pk_bf16_f32 v8, v8, v9
	v_add_f32_e32 v12, 1.0, v12
	v_add_f32_e32 v13, 1.0, v13
	v_rcp_f32_e32 v12, v12
	v_rcp_f32_e32 v13, v13
	s_nop 0
	v_pk_mul_f32 v[10:11], v[10:11], v[12:13]
	s_nop 0
	v_pk_mul_f32 v[10:11], v[14:15], v[10:11]
	s_nop 0
	v_cvt_pk_bf16_f32 v9, v10, v11
	v_mul_f32_e32 v10, 0xbfb8aa3b, v0
	v_mul_f32_e32 v11, 0xbfb8aa3b, v1
	v_exp_f32_e32 v10, v10
	v_exp_f32_e32 v11, v11
	v_add_f32_e32 v10, 1.0, v10
	v_add_f32_e32 v11, 1.0, v11
	v_rcp_f32_e32 v10, v10
	v_rcp_f32_e32 v11, v11
	s_nop 0
	v_pk_mul_f32 v[0:1], v[0:1], v[10:11]
	s_nop 0
	v_pk_mul_f32 v[0:1], v[4:5], v[0:1]
	v_mul_f32_e32 v4, 0xbfb8aa3b, v2
	v_mul_f32_e32 v5, 0xbfb8aa3b, v3
	v_exp_f32_e32 v4, v4
	v_exp_f32_e32 v5, v5
	v_cvt_pk_bf16_f32 v10, v0, v1
	v_lshlrev_b64 v[0:1], 10, v[144:145]
	v_add_f32_e32 v4, 1.0, v4
	v_add_f32_e32 v5, 1.0, v5
	v_rcp_f32_e32 v4, v4
	v_rcp_f32_e32 v5, v5
	v_permlane16_swap_b32_e32 v8, v10
	v_lshl_add_u64 v[0:1], v[80:81], 0, v[0:1]
	v_pk_mul_f32 v[2:3], v[2:3], v[4:5]
	s_nop 0
	v_pk_mul_f32 v[2:3], v[6:7], v[2:3]
	s_nop 0
	v_cvt_pk_bf16_f32 v11, v2, v3
	s_nop 1
	v_permlane16_swap_b32_e32 v9, v11
	global_store_dwordx4 v[0:1], v[8:11], off sc0 sc1
	s_waitcnt vmcnt(0)
	s_barrier
	s_cmp_lg_u32 s33, 0
	s_cbranch_scc1 .Lfuse_sig_done
	s_lshr_b32 s20, s16, 6
	s_lshl_b32 s20, s20, 3
	s_and_b32 s21, s16, 7
	s_or_b32 s20, s20, s21
	s_mul_i32 s21, s60, 129
	s_add_u32 s20, s20, s21
	s_sub_u32 s22, s4, 0x1e79fd00
	s_subb_u32 s23, s5, 0
	s_lshl_b32 s21, s20, 2
	s_add_u32 s22, s22, s21
	s_addc_u32 s23, s23, 0
	v_mov_b32_e32 v184, s22
	v_mov_b32_e32 v185, s23
	v_mov_b32_e32 v186, 1
	s_mov_b64 s[24:25], exec
	s_mov_b64 exec, 1
	s_nop 4
	flat_atomic_add v[184:185], v186
	s_mov_b64 exec, s[24:25]

.LBB0_1004:
	s_waitcnt vmcnt(0) lgkmcnt(0)
	s_branch .LBB0_1048
.LBB0_1048:
	s_or_b64 exec, exec, s[64:65]
	s_mov_b32 s0, s37
	s_waitcnt lgkmcnt(0)
	s_barrier
	s_mov_b32 s1, s33
	v_mbcnt_lo_u32_b32 v0, -1, s0
	v_mbcnt_hi_u32_b32 v0, -1, v0
	v_lshl_or_b32 v0, s1, 6, v0
	v_readlane_b32 s0, v254, 0
	s_mov_b32 s16, s0
	s_mov_b32 s0, s37
	s_add_i32 s0, s0, 0x20120
	v_mov_b32_e32 v1, s0
	s_mov_b32 s0, 0
	ds_read_b64 v[2:3], v1
	s_add_i32 s0, s0, 0x200f0
	v_mov_b32_e32 v1, s0
	s_mov_b32 s4, s60
	s_mov_b32 s5, 0
	ds_read_b64 v[4:5], v1
	s_add_i32 s5, s5, 0x20120
	v_readlane_b32 s1, v254, 1
	v_mov_b32_e32 v1, s5
	s_mov_b32 s5, 0
	s_waitcnt lgkmcnt(0)
	v_readfirstlane_b32 s1, v3
	v_readfirstlane_b32 s0, v2
	ds_read_b64 v[2:3], v1
	s_add_i32 s5, s5, 0x20120
	v_mov_b32_e32 v1, s5
	v_readlane_b32 s5, v255, 10
	v_readfirstlane_b32 s2, v5
	v_readfirstlane_b32 s6, v4
	ds_read_b64 v[4:5], v1
	v_mov_b32_e32 v1, s5
	ds_read_b32 v158, v1
	s_waitcnt lgkmcnt(0)
	v_readfirstlane_b32 s7, v3
	v_readfirstlane_b32 s11, v2
	v_readfirstlane_b32 s9, v5
	v_readfirstlane_b32 s8, v4
	v_readfirstlane_b32 s5, v158
	s_lshl_b32 s5, s5, 4
	s_addk_i32 s5, 0x70
	s_and_b32 s17, s5, 0xffffff80
	s_cmp_ge_i32 s16, s17
	v_readfirstlane_b32 s10, v0
	s_cbranch_scc1 .LBB0_1055
	v_readfirstlane_b32 s30, v158
	s_mov_b32 s26, 0
	s_mov_b32 s27, 0
	s_mov_b32 s28, 0
	s_mov_b32 s29, 0
	s_lshr_b32 s31, s16, 6
	s_bfe_u32 s38, s16, 0x30003
	s_and_b32 s39, s16, 7
	s_sub_i32 s32, s30, 64
	s_max_i32 s32, s32, 0
	s_min_i32 s32, s32, 8
	s_lshl_b32 s35, s32, 3
	s_add_u32 s29, s29, s35
	s_cmp_lt_u32 s31, 1
	s_cbranch_scc1 .Lremap_g0_notbelow
	s_add_u32 s28, s28, s35
.Lremap_g0_notbelow:
	s_cmp_lg_u32 s31, 0
	s_cbranch_scc1 .Lremap_g0_done
	s_mul_i32 s35, s38, s32
	s_add_u32 s28, s28, s35
	s_min_u32 s35, s39, s32
	s_add_u32 s28, s28, s35
	s_cmp_lt_u32 s39, s32
	s_cselect_b32 s27, 1, 0
.Lremap_g0_done:
	s_sub_i32 s32, s30, 72
	s_max_i32 s32, s32, 0
	s_min_i32 s32, s32, 8
	s_lshl_b32 s35, s32, 3
	s_add_u32 s29, s29, s35
	s_cmp_lt_u32 s31, 2
	s_cbranch_scc1 .Lremap_g1_notbelow
	s_add_u32 s28, s28, s35
.Lremap_g1_notbelow:
	s_cmp_lg_u32 s31, 1
	s_cbranch_scc1 .Lremap_g1_done
	s_mul_i32 s35, s38, s32
	s_add_u32 s28, s28, s35
	s_min_u32 s35, s39, s32
	s_add_u32 s28, s28, s35
	s_cmp_lt_u32 s39, s32
	s_cselect_b32 s27, 1, 0
.Lremap_g1_done:
	s_sub_i32 s32, s30, 80
	s_max_i32 s32, s32, 0
	s_min_i32 s32, s32, 8
	s_lshl_b32 s35, s32, 3
	s_add_u32 s29, s29, s35
	s_cmp_lt_u32 s31, 3
	s_cbranch_scc1 .Lremap_g2_notbelow
	s_add_u32 s28, s28, s35
.Lremap_g2_notbelow:
	s_cmp_lg_u32 s31, 2
	s_cbranch_scc1 .Lremap_g2_done
	s_mul_i32 s35, s38, s32
	s_add_u32 s28, s28, s35
	s_min_u32 s35, s39, s32
	s_add_u32 s28, s28, s35
	s_cmp_lt_u32 s39, s32
	s_cselect_b32 s27, 1, 0
.Lremap_g2_done:
	s_sub_i32 s32, s30, 88
	s_max_i32 s32, s32, 0
	s_min_i32 s32, s32, 8
	s_lshl_b32 s35, s32, 3
	s_add_u32 s29, s29, s35
	s_cmp_lt_u32 s31, 4
	s_cbranch_scc1 .Lremap_g3_notbelow
	s_add_u32 s28, s28, s35
.Lremap_g3_notbelow:
	s_cmp_lg_u32 s31, 3
	s_cbranch_scc1 .Lremap_g3_done
	s_mul_i32 s35, s38, s32
	s_add_u32 s28, s28, s35
	s_min_u32 s35, s39, s32
	s_add_u32 s28, s28, s35
	s_cmp_lt_u32 s39, s32
	s_cselect_b32 s27, 1, 0
.Lremap_g3_done:
	s_sub_u32 s28, s16, s28
	s_sub_u32 s29, 0x100, s29
	s_add_u32 s0, s0, 0x2779fd00
	s_addc_u32 s1, s1, 0
	s_ashr_i32 s5, s4, 31
	s_lshl_b64 s[4:5], s[4:5], 28
	s_add_u32 s4, s6, s4
	s_addc_u32 s5, s2, s5
	s_add_u32 s6, s11, 0x29b9fd00
	s_addc_u32 s7, s7, 0
	s_add_u32 s8, s8, 0x1e76bd00
	s_addc_u32 s9, s9, 0
	s_and_b32 s2, s10, 64
	v_and_b32_e32 v1, 15, v0
	v_or_b32_e32 v2, s2, v1
	s_ashr_i32 s11, s10, 7
	v_lshlrev_b32_e32 v3, 7, v2
	s_mulk_i32 s11, 0x50
	v_bfe_u32 v2, v0, 4, 2
	v_and_b32_e32 v4, 7, v0
	v_or_b32_e32 v160, s11, v1
	v_and_b32_e32 v1, 63, v0
	v_bitop3_b32 v4, v2, v4, 4 bitop3:0x36
	v_bitop3_b32 v2, v2, v0, 7 bitop3:0x78
	v_lshlrev_b32_e32 v162, 4, v2
	v_lshlrev_b32_e32 v2, 1, v1
	v_lshlrev_b32_e32 v161, 4, v4
	s_ashr_i32 s10, s10, 6
	v_or_b32_e32 v4, 1, v2
	v_bitop3_b32 v5, s10, v4, 7 bitop3:0x78
	v_lshlrev_b32_e32 v4, 7, v4
	v_ashrrev_i32_e32 v159, 3, v0
	v_lshl_add_u32 v163, v5, 4, v4
	v_bitop3_b32 v4, s10, v2, 6 bitop3:0x78
	v_lshlrev_b32_e32 v1, 8, v1
	v_lshl_add_u32 v164, v4, 4, v1
	v_xor_b32_e32 v1, v159, v0
	v_lshlrev_b32_e32 v1, 4, v1
	v_lshlrev_b32_e32 v4, 7, v159
	s_movk_i32 s11, 0x70
	v_and_or_b32 v1, v1, s11, v4
	v_lshlrev_b32_e32 v4, 3, v0
	s_lshl_b32 s10, s10, 3
	v_and_b32_e32 v6, 16, v0
	v_lshrrev_b32_e32 v0, 2, v0
	v_and_b32_e32 v4, 56, v4
	s_ashr_i32 s11, s10, 31
	v_add_u32_e32 v165, 0, v1
	s_add_i32 s18, 0, 0x18000
	v_and_b32_e32 v0, 8, v0
	s_lshl_b64 s[10:11], s[10:11], 13
	v_add_u32_e32 v166, s66, v3
	v_lshl_add_u32 v167, v160, 7, 0
	v_add_u32_e32 v168, 0xa000, v165
	v_add_u32_e32 v169, s18, v3
	v_lshlrev_b32_e32 v100, 1, v4
	v_lshlrev_b32_e32 v102, 2, v2
	s_lshl_b32 s19, s2, 1
	v_lshlrev_b32_e32 v104, 1, v6
	v_lshlrev_b32_e32 v106, 1, v0
	v_mbcnt_lo_u32_b32 v184, -1, 0
	v_mbcnt_hi_u32_b32 v184, -1, v184
	v_and_b32_e32 v185, 31, v184
	v_lshrrev_b32_e32 v186, 5, v184
	v_lshlrev_b32_e32 v187, 4, v185
	v_lshl_add_u32 v102, v186, 15, v187
	v_lshlrev_b32_e32 v188, 2, v185
	v_lshl_add_u32 v188, v186, 1, v188
	v_and_b32_e32 v189, 7, v188
	v_xor_b32_e32 v189, s33, v189
	v_lshlrev_b32_e32 v189, 4, v189
	v_lshl_add_u32 v164, v188, 7, v189
	v_add_u32_e32 v188, 1, v188
	v_and_b32_e32 v189, 7, v188
	v_xor_b32_e32 v189, s33, v189
	v_lshlrev_b32_e32 v189, 4, v189
	v_lshl_add_u32 v163, v188, 7, v189
	s_branch .LBB0_1051
.LBB0_1050:
	s_add_u32 s26, s26, 1
	s_cmp_lt_u32 s26, 3
	s_cbranch_scc0 .Lremap_extra
	s_addk_i32 s16, 0x100
	s_branch .Lremap_check
.Lremap_extra:
	s_cmp_eq_u32 s27, 1
	s_cbranch_scc1 .LBB0_1055
	s_cmp_eq_u32 s26, 3
	s_cbranch_scc0 .Lremap_next
	s_add_u32 s16, s28, 768
	s_branch .Lremap_check
.Lremap_next:
	s_add_u32 s16, s16, s29
.Lremap_check:
	s_cmp_lt_i32 s16, s17
	s_cbranch_scc0 .LBB0_1055
.LBB0_1051:
	s_ashr_i32 s2, s16, 31
	s_lshr_b32 s2, s2, 25
	s_add_i32 s2, s16, s2
	s_ashr_i32 s12, s2, 7
	s_and_b32 s2, s2, 0xffffff80
	s_sub_i32 s2, s16, s2
	s_lshl_b32 s12, s12, 3
	s_and_b32 s13, s2, 7
	s_or_b32 s20, s12, s13
	v_cmp_ge_i32_e32 vcc, s20, v158
	s_cbranch_vccnz .LBB0_1050
	s_sub_u32 s22, s0, 0x2779fd00
	s_subb_u32 s23, s1, 0
	s_mul_i32 s24, s60, 129
	s_add_u32 s24, s24, s20
	s_lshl_b32 s24, s24, 2
	s_add_u32 s22, s22, s24
	s_addc_u32 s23, s23, 0
	s_mov_b32 s24, 8
	s_mov_b32 s100, 0
	v_mov_b32_e32 v184, s22
	v_mov_b32_e32 v185, s23
	s_cmp_lg_u32 s33, 0
	s_cbranch_scc1 .Lfuse_ready2
.Lfuse_wait:
	flat_load_dword v186, v[184:185] sc1
	s_waitcnt vmcnt(0) lgkmcnt(0)
	v_readfirstlane_b32 s25, v186
	s_nop 3
	s_cmp_ge_u32 s25, s24
	s_cbranch_scc1 .Lfuse_ready
	s_add_u32 s100, s100, 1
	s_cmp_gt_u32 s100, 0x40000
	s_cbranch_scc1 .Lfuse_ready
	s_sleep 16
	s_branch .Lfuse_wait
.Lfuse_ready:
	buffer_inv sc1
	s_waitcnt vmcnt(0)
.Lfuse_ready2:
	s_barrier
	s_lshl_b32 s12, s20, 2
	s_add_i32 s12, s12, 0
	s_add_i32 s12, s12, 0x20b40
	v_mov_b32_e32 v0, s12
	v_mov_b32_e32 v2, v145
	s_mulk_i32 s20, 0x140
	ds_read_b32 v0, v0
	s_mov_b64 s[12:13], s[0:1]
	s_mov_b64 s[22:23], 0
	s_mov_b64 s[24:25], s[4:5]
	v_add3_u32 v144, s20, v159, v2
	s_mul_i32 s14, s2, 5
	v_lshlrev_b64 v[4:5], 10, v[144:145]
	s_lshl_b32 s2, s2, 4
	v_lshl_add_u64 v[4:5], s[12:13], 0, v[4:5]
	v_mov_b32_e32 v101, v145
	s_and_b32 s12, s2, 0xffffff80
	s_and_b32 s2, s14, 7
	v_lshl_add_u64 v[108:109], v[4:5], 0, v[100:101]
	s_lshl_b32 s36, s2, 7
	v_lshl_add_u64 v[16:17], v[108:109], 0, s[36:37]
	s_waitcnt lgkmcnt(0)
	v_ashrrev_i32_e32 v1, 31, v0
	v_add_co_u32_e32 v4, vcc, s70, v16
	v_lshlrev_b64 v[0:1], 22, v[0:1]
	s_ashr_i32 s13, s12, 31
	v_addc_co_u32_e32 v5, vcc, 0, v17, vcc
	v_lshl_add_u64 v[0:1], s[24:25], 0, v[0:1]
	s_lshl_b64 s[22:23], s[12:13], 2
	v_add_co_u32_e32 v8, vcc, s83, v16
	v_lshl_add_u64 v[0:1], v[0:1], 0, s[22:23]
	v_mov_b32_e32 v103, v145
	v_addc_co_u32_e32 v9, vcc, 0, v17, vcc
	v_lshl_add_u64 v[0:1], v[0:1], 0, v[102:103]
	v_ashrrev_i32_e32 v3, 31, v2
	v_add_co_u32_e32 v12, vcc, s3, v16
	v_lshl_add_u64 v[0:1], v[2:3], 2, v[0:1]
	s_nop 0
	v_addc_co_u32_e32 v13, vcc, 0, v17, vcc
	v_lshl_add_u64 v[110:111], v[0:1], 0, s[10:11]
	v_add_u32_e32 v200, s20, v160
	v_mov_b32_e32 v201, v145
	v_lshl_add_u64 v[202:203], v[200:201], 2, s[8:9]
	global_load_dword v190, v[202:203], off
	global_load_dword v192, v[202:203], off offset:64
	global_load_dword v194, v[202:203], off offset:128
	global_load_dword v196, v[202:203], off offset:192
	global_load_dword v198, v[202:203], off offset:256
	global_load_dwordx4 v[0:3], v[16:17], off
	s_nop 0
	global_load_dwordx4 v[4:7], v[4:5], off
	v_add_co_u32_e32 v16, vcc, s53, v16
	s_lshl_b32 s36, s2, 19
	s_nop 0
	v_addc_co_u32_e32 v17, vcc, 0, v17, vcc
	global_load_dwordx4 v[8:11], v[8:9], off
	s_nop 0
	global_load_dwordx4 v[12:15], v[12:13], off
	global_load_dwordx4 v[16:19], v[16:17], off
	v_lshl_add_u64 v[32:33], v[110:111], 0, s[36:37]
	v_add_co_u32_e32 v34, vcc, 0x2000, v32
	s_nop 1
	v_addc_co_u32_e32 v35, vcc, 0, v33, vcc
	v_add_co_u32_e32 v28, vcc, 0x4000, v32
	s_nop 1
	v_addc_co_u32_e32 v29, vcc, 0, v33, vcc
	v_add_co_u32_e32 v30, vcc, 0x6000, v32
	s_nop 1
	v_addc_co_u32_e32 v31, vcc, 0, v33, vcc
	global_load_dwordx4 v[20:23], v[32:33], off
	global_load_dwordx4 v[24:27], v[34:35], off
	global_load_dwordx4 v[32:35], v[30:31], off
	global_load_dwordx4 v[28:31], v[28:29], off
	s_nop 0
	s_add_i32 s2, s14, 1
	s_nop 0
	s_nop 0
	s_nop 0
	s_nop 0
	s_and_b32 s2, s2, 7
	s_nop 0
	s_lshl_b32 s36, s2, 19
	s_nop 0
	s_nop 0
	s_nop 0
	s_nop 0
	s_nop 0
	v_lshl_add_u64 v[124:125], v[110:111], 0, s[36:37]
	v_add_co_u32_e32 v126, vcc, 0x2000, v124
	s_nop 1
	v_addc_co_u32_e32 v127, vcc, 0, v125, vcc
	v_add_co_u32_e32 v120, vcc, 0x4000, v124
	s_nop 1
	v_addc_co_u32_e32 v121, vcc, 0, v125, vcc
	v_add_co_u32_e32 v122, vcc, 0x6000, v124
	s_nop 1
	v_addc_co_u32_e32 v123, vcc, 0, v125, vcc
	global_load_dwordx4 v[112:115], v[124:125], off
	global_load_dwordx4 v[116:119], v[126:127], off
	global_load_dwordx4 v[124:127], v[122:123], off
	global_load_dwordx4 v[120:123], v[120:121], off
	v_add_u32_e32 v101, s66, v164
	s_nop 0
	s_lshl_b32 s36, s2, 7
	s_nop 0
	v_add_u32_e32 v103, s66, v163
	s_nop 0
	v_mov_b32_e32 v64, 0
	s_nop 0
	s_mov_b32 s15, -2
	s_nop 0
	v_mov_b32_e32 v65, v64
	s_nop 0
	v_mov_b32_e32 v66, v64
	s_nop 0
	s_waitcnt vmcnt(0)
	ds_write_b128 v165, v[0:3]
	ds_write_b128 v165, v[4:7] offset:8192
	ds_write_b128 v165, v[8:11] offset:16384
	ds_write_b128 v165, v[12:15] offset:24576
	ds_write_b128 v165, v[16:19] offset:32768
	v_mov_b32_e32 v67, v64
	v_mov_b32_e32 v68, v64
	v_mov_b32_e32 v69, v64
	v_mov_b32_e32 v70, v64
	v_mov_b32_e32 v71, v64
	v_mov_b32_e32 v72, v64
	v_mov_b32_e32 v73, v64
	v_mov_b32_e32 v74, v64
	v_mov_b32_e32 v75, v64
	v_mov_b32_e32 v76, v64
	v_mov_b32_e32 v77, v64
	v_permlane32_swap_b32_e32 v20, v22
	v_permlane32_swap_b32_e32 v21, v23
	v_permlane32_swap_b32_e32 v24, v26
	v_permlane32_swap_b32_e32 v25, v27
	v_permlane32_swap_b32_e32 v28, v30
	v_permlane32_swap_b32_e32 v29, v31
	v_permlane32_swap_b32_e32 v32, v34
	v_permlane32_swap_b32_e32 v33, v35
	v_cvt_pk_bf16_f32 v0, v20, v24
	v_cvt_pk_bf16_f32 v1, v28, v32
	v_cvt_pk_bf16_f32 v2, v22, v26
	v_cvt_pk_bf16_f32 v3, v30, v34
	v_cvt_pk_bf16_f32 v4, v21, v25
	v_cvt_pk_bf16_f32 v5, v29, v33
	v_cvt_pk_bf16_f32 v6, v23, v27
	v_cvt_pk_bf16_f32 v7, v31, v35
	v_mov_b32_e32 v78, v64
	v_mov_b32_e32 v79, v64
	v_mov_b32_e32 v48, v64
	v_mov_b32_e32 v49, v64
	v_mov_b32_e32 v50, v64
	v_mov_b32_e32 v51, v64
	v_mov_b32_e32 v52, v64
	v_mov_b32_e32 v53, v64
	v_mov_b32_e32 v54, v64
	v_mov_b32_e32 v55, v64
	v_mov_b32_e32 v56, v64
	v_mov_b32_e32 v57, v64
	v_mov_b32_e32 v58, v64
	v_mov_b32_e32 v59, v64
	ds_write_b128 v101, v[0:3]
	v_lshl_add_u64 v[0:1], v[108:109], 0, s[36:37]
	v_add_co_u32_e32 v2, vcc, s70, v0
	ds_write_b128 v103, v[4:7]
	s_nop 0
	v_addc_co_u32_e32 v3, vcc, 0, v1, vcc
	global_load_dwordx4 v[80:83], v[0:1], off
	global_load_dwordx4 v[84:87], v[2:3], off
	v_add_co_u32_e32 v2, vcc, s83, v0
	v_mov_b32_e32 v60, v64
	s_nop 0
	v_addc_co_u32_e32 v3, vcc, 0, v1, vcc
	v_add_co_u32_e32 v4, vcc, 0x30000, v0
	v_mov_b32_e32 v61, v64
	s_nop 0
	v_addc_co_u32_e32 v5, vcc, 0, v1, vcc
	v_add_co_u32_e32 v0, vcc, 0x40000, v0
	global_load_dwordx4 v[88:91], v[2:3], off
	global_load_dwordx4 v[92:95], v[4:5], off
	v_addc_co_u32_e32 v1, vcc, 0, v1, vcc
	global_load_dwordx4 v[96:99], v[0:1], off
	v_mov_b32_e32 v62, v64
	v_mov_b32_e32 v63, v64
	v_mov_b32_e32 v32, v64
	v_mov_b32_e32 v33, v64
	v_mov_b32_e32 v34, v64
	v_mov_b32_e32 v35, v64
	v_mov_b32_e32 v36, v64
	v_mov_b32_e32 v37, v64
	v_mov_b32_e32 v38, v64
	v_mov_b32_e32 v39, v64
	v_mov_b32_e32 v40, v64
	v_mov_b32_e32 v41, v64
	v_mov_b32_e32 v42, v64
	v_mov_b32_e32 v43, v64
	v_mov_b32_e32 v44, v64
	v_mov_b32_e32 v45, v64
	v_mov_b32_e32 v46, v64
	v_mov_b32_e32 v47, v64
	v_mov_b32_e32 v16, v64
	v_mov_b32_e32 v17, v64
	v_mov_b32_e32 v18, v64
	v_mov_b32_e32 v19, v64
	v_mov_b32_e32 v20, v64
	v_mov_b32_e32 v21, v64
	v_mov_b32_e32 v22, v64
	v_mov_b32_e32 v23, v64
	v_mov_b32_e32 v24, v64
	v_mov_b32_e32 v25, v64
	v_mov_b32_e32 v26, v64
	v_mov_b32_e32 v27, v64
	v_mov_b32_e32 v28, v64
	v_mov_b32_e32 v29, v64
	v_mov_b32_e32 v30, v64
	v_mov_b32_e32 v31, v64
	v_mov_b32_e32 v0, v64
	v_mov_b32_e32 v1, v64
	v_mov_b32_e32 v2, v64
	v_mov_b32_e32 v3, v64
	v_mov_b32_e32 v4, v64
	v_mov_b32_e32 v5, v64
	v_mov_b32_e32 v6, v64
	v_mov_b32_e32 v7, v64
	v_mov_b32_e32 v8, v64
	v_mov_b32_e32 v9, v64
	v_mov_b32_e32 v10, v64
	v_mov_b32_e32 v11, v64
	v_mov_b32_e32 v12, v64
	v_mov_b32_e32 v13, v64
	v_mov_b32_e32 v14, v64
	v_mov_b32_e32 v15, v64
	s_waitcnt lgkmcnt(0)
	s_barrier

	.amdhsa_kernel _ZN12_GLOBAL__N_14megaENS_6ParamsE
		.amdhsa_group_segment_fixed_size 0
		.amdhsa_private_segment_fixed_size 0
		.amdhsa_kernarg_size 536
		.amdhsa_user_sgpr_count 2
		.amdhsa_user_sgpr_dispatch_ptr 0
		.amdhsa_user_sgpr_queue_ptr 0
		.amdhsa_user_sgpr_kernarg_segment_ptr 1
		.amdhsa_user_sgpr_dispatch_id 0
		.amdhsa_user_sgpr_kernarg_preload_length 0
		.amdhsa_user_sgpr_kernarg_preload_offset 0
		.amdhsa_user_sgpr_private_segment_size 0
		.amdhsa_uses_dynamic_stack 0
		.amdhsa_enable_private_segment 0
		.amdhsa_system_sgpr_workgroup_id_x 1
		.amdhsa_system_sgpr_workgroup_id_y 0
		.amdhsa_system_sgpr_workgroup_id_z 0
		.amdhsa_system_sgpr_workgroup_info 0
		.amdhsa_system_vgpr_workitem_id 0
		.amdhsa_next_free_vgpr 256
		.amdhsa_next_free_sgpr 102
		.amdhsa_accum_offset 256
		.amdhsa_reserve_vcc 1
		.amdhsa_float_round_mode_32 0
		.amdhsa_float_round_mode_16_64 0
		.amdhsa_float_denorm_mode_32 3
		.amdhsa_float_denorm_mode_16_64 3
		.amdhsa_dx10_clamp 1
		.amdhsa_ieee_mode 1
		.amdhsa_fp16_overflow 0
		.amdhsa_tg_split 0
		.amdhsa_exception_fp_ieee_invalid_op 0
		.amdhsa_exception_fp_denorm_src 0
		.amdhsa_exception_fp_ieee_div_zero 0
		.amdhsa_exception_fp_ieee_overflow 0
		.amdhsa_exception_fp_ieee_underflow 0
		.amdhsa_exception_fp_ieee_inexact 0
		.amdhsa_exception_int_div_zero 0
	.end_amdhsa_kernel

amdhsa.kernels:
  - .agpr_count:     0
    .args:
      - .offset:         0
        .size:           280
        .value_kind:     by_value
      - .offset:         280
        .size:           4
        .value_kind:     hidden_block_count_x
      - .offset:         284
        .size:           4
        .value_kind:     hidden_block_count_y
      - .offset:         288
        .size:           4
        .value_kind:     hidden_block_count_z
      - .offset:         292
        .size:           2
        .value_kind:     hidden_group_size_x
      - .offset:         294
        .size:           2
        .value_kind:     hidden_group_size_y
      - .offset:         296
        .size:           2
        .value_kind:     hidden_group_size_z
      - .offset:         298
        .size:           2
        .value_kind:     hidden_remainder_x
      - .offset:         300
        .size:           2
        .value_kind:     hidden_remainder_y
      - .offset:         302
        .size:           2
        .value_kind:     hidden_remainder_z
      - .offset:         320
        .size:           8
        .value_kind:     hidden_global_offset_x
      - .offset:         328
        .size:           8
        .value_kind:     hidden_global_offset_y
      - .offset:         336
        .size:           8
        .value_kind:     hidden_global_offset_z
      - .offset:         344
        .size:           2
        .value_kind:     hidden_grid_dims
      - .offset:         400
        .size:           4
        .value_kind:     hidden_dynamic_lds_size
    .group_segment_fixed_size: 0
    .kernarg_segment_align: 8
    .kernarg_segment_size: 536
    .language:       OpenCL C
    .language_version:
      - 2
      - 0
    .max_flat_workgroup_size: 512
    .name:           _ZN12_GLOBAL__N_14megaENS_6ParamsE
    .private_segment_fixed_size: 0
    .sgpr_count:     108
    .sgpr_spill_count: 80
    .symbol:         _ZN12_GLOBAL__N_14megaENS_6ParamsE.kd
    .uniform_work_group_size: 1
    .uses_dynamic_stack: false
    .vgpr_count:     256
    .vgpr_spill_count: 0
    .wavefront_size: 64
